# GQA plain loop: the 32 per-trip score copies removed (step 2 loads its key fragments with the halves swapped so its MFMAs write the scores where step 1 reads them)
# speedup vs baseline: 1.0144x; 1.0046x over previous
; DI f32x16 mfma8(v8i a, v8i b, f32x16 c) { return __builtin_amdgcn_mfma_scale_f32_32x32x64_f8f6f4(a, b, c, 0, 0, 0, 0, 0, 0); }
; DI void attn_unit_a8(unsigned char* lds, const AttnArgs& a) {
;     ...
;     auto step = [&](int t, u32x2& kl, u32x2& vl, const u32x2& ks, const u32x2& vs, f32x16& c0, f32x16& c1, f32x16& n0, f32x16& n1, const int hk, const int wj) __attribute__((always_inline)) {
;         const int slot1 = slot == 2 ? 0 : slot + 1, slot2 = slot1 == 2 ? 0 : slot1 + 1;
;         if (hk == 1) { w_cvt(); w_issue(wj + 1 < AT_NWT ? wj + 1 : AT_NWT - 1); }
;         if (hk == 2) w_store(wj);
;         { const int tn = t + 3; gload(tn < a.t1 ? tn : a.t1 - 1, kl, vl); }
;         const unsigned char* Kb = lds + slot * AT_BUFB; const unsigned char* Kn = lds + slot1 * AT_BUFB;
;         const v8i k0 = kread(Kn, 0), k1 = kread(Kn, 1), v0 = vread(Kb, 0), v1 = vread(Kb, 1);
;         n0 = mfma8(k0, qf8, cinit); n1 = mfma8(k1, qf8, cinit);
;         expsum(c0); expsum(c1);
;         const v8i P = pack8(c0, c1);
;         o0[0] = mfma8(v0, P, o0[0]); o0[1] = mfma8(v1, P, o0[1]);
;         lstore(slot2, ks, vs);
;         __syncthreads();
;         slot = slot1;
;     };
.LBB0_712:
	s_cmpk_gt_i32 s56, 0x43
	s_cbranch_scc1 .LBB0_688
	s_mov_b32 s8, 0
	v_mov_b64_e32 v[80:81], v[48:49]
	v_mov_b64_e32 v[78:79], v[46:47]
	v_mov_b64_e32 v[76:77], v[44:45]
	v_mov_b64_e32 v[74:75], v[42:43]
	v_mov_b64_e32 v[72:73], v[40:41]
	v_mov_b64_e32 v[70:71], v[38:39]
	v_mov_b64_e32 v[68:69], v[36:37]
	v_mov_b64_e32 v[66:67], v[34:35]
	v_mov_b64_e32 v[96:97], v[64:65]
	v_mov_b64_e32 v[94:95], v[62:63]
	v_mov_b64_e32 v[92:93], v[60:61]
	v_mov_b64_e32 v[90:91], v[58:59]
	v_mov_b64_e32 v[88:89], v[56:57]
	v_mov_b64_e32 v[86:87], v[54:55]
	v_mov_b64_e32 v[84:85], v[52:53]
	v_mov_b64_e32 v[82:83], v[50:51]
.LBB0_714:
	s_min_i32 s4, s56, 64
	s_add_i32 s6, s4, 3
	s_cmp_lt_u32 s56, 61
	s_cselect_b64 s[10:11], -1, 0
	s_lshl_b32 s4, s6, 6
	s_add_i32 s7, s4, 0xfffff000
	s_and_b64 s[12:13], s[10:11], exec
	s_nop 0
	s_cselect_b32 s4, s4, s7
	s_nop 0
	s_nop 0
	s_nop 0
	s_nop 0
	s_nop 0
	s_nop 0
	s_nop 0
	v_add_u32_e32 v42, s4, v154
	s_add_i32 s4, s8, 1
	s_cmp_lg_u32 s8, 2
	s_mov_b32 s9, s8
	s_cselect_b32 s8, s4, 0
	s_mul_i32 s4, s8, 0x4680
	v_add_u32_e32 v106, s4, v157
	ds_read_b128 v[34:37], v106
	ds_read_b128 v[38:41], v106 offset:16
	s_nop 0
	s_and_b64 s[10:11], s[10:11], exec
	v_ashrrev_i32_e32 v43, 31, v42
	s_nop 0
	s_nop 0
	s_nop 0
	s_nop 0
	s_nop 0
	s_nop 0
	s_nop 0
	s_cselect_b32 s10, s58, s60
	s_cselect_b32 s11, s59, s61
	s_ashr_i32 s7, s6, 31
	s_waitcnt lgkmcnt(0)
	v_mfma_f32_32x32x64_f8f6f4 v[50:65], v[34:41], v[98:105], 0
	v_lshlrev_b64 v[34:35], 7, v[42:43]
	s_lshl_b64 s[12:13], s[6:7], 6
	v_lshl_add_u64 v[34:35], s[10:11], 0, v[34:35]
	v_lshl_add_u64 v[34:35], v[34:35], 0, v[130:131]
	v_lshl_add_u64 v[42:43], v[132:133], 0, s[12:13]
	global_load_dwordx2 v[112:113], v[34:35], off
	ds_read_b128 v[34:37], v106 offset:2560
	ds_read_b128 v[38:41], v106 offset:2576
	global_load_dwordx2 v[114:115], v[42:43], off
	s_mulk_i32 s9, 0x4680
	v_add_u32_e32 v42, s9, v157
	v_exp_f32_e32 v82, v82
	v_exp_f32_e32 v83, v83
	v_exp_f32_e32 v86, v86
	v_exp_f32_e32 v87, v87
	v_exp_f32_e32 v90, v90
	v_exp_f32_e32 v91, v91
	v_exp_f32_e32 v94, v94
	v_exp_f32_e32 v95, v95
	v_exp_f32_e32 v124, v66
	v_exp_f32_e32 v125, v67
	v_exp_f32_e32 v146, v70
	v_exp_f32_e32 v147, v71
	v_exp_f32_e32 v74, v74
	v_exp_f32_e32 v75, v75
	v_exp_f32_e32 v78, v78
	v_exp_f32_e32 v79, v79
	ds_read_b128 v[116:119], v42 offset:5120
	ds_read_b128 v[120:123], v42 offset:5136
	ds_read_b128 v[138:141], v42 offset:7680
	ds_read_b128 v[142:145], v42 offset:7696
	v_exp_f32_e32 v84, v84
	v_exp_f32_e32 v85, v85
	v_exp_f32_e32 v88, v88
	v_exp_f32_e32 v89, v89
	v_exp_f32_e32 v92, v92
	v_exp_f32_e32 v93, v93
	v_exp_f32_e32 v96, v96
	v_exp_f32_e32 v97, v97
	v_exp_f32_e32 v126, v68
	v_exp_f32_e32 v127, v69
	v_exp_f32_e32 v148, v72
	v_exp_f32_e32 v149, v73
	v_exp_f32_e32 v76, v76
	v_exp_f32_e32 v77, v77
	v_exp_f32_e32 v80, v80
	v_exp_f32_e32 v81, v81
	s_nop 0
	s_nop 0
	s_nop 0
	s_nop 0
	s_nop 0
	s_nop 0
	s_nop 0
	s_nop 0
	v_cvt_scalef32_pk_fp8_f32 v66, v82, v83, s48
	v_cvt_scalef32_pk_fp8_f32 v70, v124, v125, s48
	v_cvt_scalef32_pk_fp8_f32 v67, v86, v87, s48
	v_cvt_scalef32_pk_fp8_f32 v71, v146, v147, s48
	v_cvt_scalef32_pk_fp8_f32 v68, v90, v91, s48
	v_cvt_scalef32_pk_fp8_f32 v72, v74, v75, s48
	v_cvt_scalef32_pk_fp8_f32 v69, v94, v95, s48
	v_cvt_scalef32_pk_fp8_f32 v73, v78, v79, s48
	v_cvt_scalef32_pk_fp8_f32 v66, v84, v85, s48 op_sel:[0,0,0,1]
	v_cvt_scalef32_pk_fp8_f32 v70, v126, v127, s48 op_sel:[0,0,0,1]
	v_cvt_scalef32_pk_fp8_f32 v67, v88, v89, s48 op_sel:[0,0,0,1]
	v_cvt_scalef32_pk_fp8_f32 v71, v148, v149, s48 op_sel:[0,0,0,1]
	v_cvt_scalef32_pk_fp8_f32 v68, v92, v93, s48 op_sel:[0,0,0,1]
	v_cvt_scalef32_pk_fp8_f32 v72, v76, v77, s48 op_sel:[0,0,0,1]
	v_cvt_scalef32_pk_fp8_f32 v69, v96, v97, s48 op_sel:[0,0,0,1]
	v_cvt_scalef32_pk_fp8_f32 v73, v80, v81, s48 op_sel:[0,0,0,1]
	s_waitcnt lgkmcnt(4)
	v_mfma_f32_32x32x64_f8f6f4 v[34:49], v[34:41], v[98:105], 0
	s_addk_i32 s4, 0x4680
	s_cmp_eq_u32 s8, 2
	v_add_f32_e64 v110, v110, v84
	v_add_f32_e64 v111, v111, v85
	v_add_f32_e64 v82, v108, v82
	v_add_f32_e64 v83, v109, v83
	s_cselect_b64 s[6:7], -1, 0
	v_add_f32_e64 v84, v88, v110
	v_add_f32_e64 v85, v89, v111
	v_add_f32_e64 v82, v86, v82
	v_add_f32_e64 v83, v87, v83
	v_add_f32_e64 v84, v92, v84
	v_add_f32_e64 v85, v93, v85
	v_pk_add_f32 v[82:83], v[90:91], v[82:83]
	s_and_b64 s[10:11], s[6:7], exec
	v_pk_add_f32 v[84:85], v[96:97], v[84:85]
	v_pk_add_f32 v[82:83], v[94:95], v[82:83]
	s_cselect_b32 s4, 0, s4
	v_pk_add_f32 v[82:83], v[124:125], v[82:83]
	v_pk_add_f32 v[84:85], v[126:127], v[84:85]
	s_waitcnt lgkmcnt(2)
	v_mfma_f32_32x32x64_f8f6f4 v[18:33], v[116:123], v[66:73], v[18:33]
	s_add_i32 s4, s4, 0
	v_add_f32_e64 v84, v148, v84
	v_add_f32_e64 v85, v149, v85
	v_add_f32_e64 v82, v146, v82
	v_add_f32_e64 v83, v147, v83
	v_add_f32_e64 v76, v76, v84
	v_add_f32_e64 v77, v77, v85
	v_add_f32_e64 v74, v74, v82
	v_add_f32_e64 v75, v75, v83
	v_add_f32_e64 v110, v80, v76
	v_add_f32_e64 v111, v81, v77
	v_add_f32_e64 v108, v78, v74
	v_add_f32_e64 v109, v79, v75
	s_cmpk_gt_u32 s56, 0x42
	s_waitcnt lgkmcnt(0)
	v_mfma_f32_32x32x64_f8f6f4 v[2:17], v[138:145], v[66:73], v[2:17]
	v_add_u32_e32 v66, s4, v155
	s_waitcnt vmcnt(3)
	ds_write_b64 v66, v[134:135]
	v_add_u32_e32 v66, s4, v156
	v_add_u32_e32 v66, 0x1400, v66
	s_waitcnt vmcnt(2)
	ds_write2_b32 v66, v136, v137 offset1:8
	s_waitcnt lgkmcnt(0)
	s_barrier
; DI f32x16 mfma8(v8i a, v8i b, f32x16 c) { return __builtin_amdgcn_mfma_scale_f32_32x32x64_f8f6f4(a, b, c, 0, 0, 0, 0, 0, 0); }
; DI void attn_unit_a8(unsigned char* lds, const AttnArgs& a) {
;     ...
;     auto step = [&](int t, u32x2& kl, u32x2& vl, const u32x2& ks, const u32x2& vs, f32x16& c0, f32x16& c1, f32x16& n0, f32x16& n1, const int hk, const int wj) __attribute__((always_inline)) {
;         const int slot1 = slot == 2 ? 0 : slot + 1, slot2 = slot1 == 2 ? 0 : slot1 + 1;
;         if (hk == 1) { w_cvt(); w_issue(wj + 1 < AT_NWT ? wj + 1 : AT_NWT - 1); }
;         if (hk == 2) w_store(wj);
;         { const int tn = t + 3; gload(tn < a.t1 ? tn : a.t1 - 1, kl, vl); }
;         const unsigned char* Kb = lds + slot * AT_BUFB; const unsigned char* Kn = lds + slot1 * AT_BUFB;
;         const v8i k0 = kread(Kn, 0), k1 = kread(Kn, 1), v0 = vread(Kb, 0), v1 = vread(Kb, 1);
;         n0 = mfma8(k0, qf8, cinit); n1 = mfma8(k1, qf8, cinit);
;         expsum(c0); expsum(c1);
;         const v8i P = pack8(c0, c1);
;         o0[0] = mfma8(v0, P, o0[0]); o0[1] = mfma8(v1, P, o0[1]);
;         lstore(slot2, ks, vs);
;         __syncthreads();
;         slot = slot1;
;     };
	s_cbranch_scc1 .LBB0_716
	s_min_u32 s4, s56, 63
	s_cmp_lt_u32 s56, 60
	s_cselect_b64 s[10:11], -1, 0
	s_lshl_b32 s4, s4, 6
	s_add_i32 s9, s4, 0x100
	s_add_i32 s14, s4, 0xfffff100
	s_and_b64 s[12:13], s[10:11], exec
	s_cselect_b32 s9, s9, s14
	s_add_i32 s8, s8, 1
	s_and_b64 s[6:7], s[6:7], exec
	v_add_u32_e32 v82, s9, v154
	s_cselect_b32 s8, 0, s8
	s_and_b64 s[10:11], s[10:11], exec
	v_ashrrev_i32_e32 v83, 31, v82
	s_cselect_b32 s11, s59, s61
	s_cselect_b32 s10, s58, s60
	v_lshlrev_b64 v[82:83], 7, v[82:83]
	s_mul_i32 s6, s8, 0x4680
	v_lshl_add_u64 v[90:91], s[10:11], 0, v[82:83]
	v_add_u32_e32 v86, s6, v157
	v_lshl_add_u64 v[90:91], v[90:91], 0, v[130:131]
	ds_read_b128 v[66:69], v86 offset:2560
	ds_read_b128 v[70:73], v86 offset:2576
	ds_read_b128 v[82:85], v86
	ds_read_b128 v[86:89], v86 offset:16
	global_load_dwordx2 v[134:135], v[90:91], off
	v_lshl_add_u64 v[90:91], v[132:133], 0, s[4:5]
	global_load_dwordx2 v[136:137], v[90:91], off offset:256
	v_exp_f32_e32 v50, v50
	v_exp_f32_e32 v51, v51
	v_exp_f32_e32 v54, v54
	v_exp_f32_e32 v55, v55
	v_exp_f32_e32 v58, v58
	v_exp_f32_e32 v59, v59
	v_exp_f32_e32 v62, v62
	v_exp_f32_e32 v63, v63
	v_exp_f32_e32 v124, v34
	v_exp_f32_e32 v125, v35
	v_exp_f32_e32 v146, v38
	v_exp_f32_e32 v147, v39
	v_exp_f32_e32 v42, v42
	v_exp_f32_e32 v43, v43
	v_exp_f32_e32 v46, v46
	v_exp_f32_e32 v47, v47
	ds_read_b128 v[116:119], v106 offset:5120
	ds_read_b128 v[120:123], v106 offset:5136
	ds_read_b128 v[138:141], v106 offset:7680
	ds_read_b128 v[142:145], v106 offset:7696
	v_exp_f32_e32 v52, v52
	v_exp_f32_e32 v53, v53
	v_exp_f32_e32 v56, v56
	v_exp_f32_e32 v57, v57
	v_exp_f32_e32 v60, v60
	v_exp_f32_e32 v61, v61
	v_exp_f32_e32 v64, v64
	v_exp_f32_e32 v65, v65
	v_exp_f32_e32 v126, v36
	v_exp_f32_e32 v127, v37
	v_exp_f32_e32 v148, v40
	v_exp_f32_e32 v149, v41
	v_exp_f32_e32 v44, v44
	v_exp_f32_e32 v45, v45
	v_exp_f32_e32 v48, v48
	v_exp_f32_e32 v49, v49
	s_nop 0
	s_nop 0
	s_nop 0
	s_nop 0
	s_nop 0
	s_nop 0
	s_nop 0
	s_nop 0
	s_waitcnt lgkmcnt(6)
	v_mfma_f32_32x32x64_f8f6f4 v[66:81], v[66:73], v[98:105], 0
	v_cvt_scalef32_pk_fp8_f32 v34, v50, v51, s48
	v_cvt_scalef32_pk_fp8_f32 v38, v124, v125, s48
	v_cvt_scalef32_pk_fp8_f32 v35, v54, v55, s48
	v_cvt_scalef32_pk_fp8_f32 v39, v146, v147, s48
	v_cvt_scalef32_pk_fp8_f32 v36, v58, v59, s48
	v_cvt_scalef32_pk_fp8_f32 v40, v42, v43, s48
	v_cvt_scalef32_pk_fp8_f32 v37, v62, v63, s48
	v_cvt_scalef32_pk_fp8_f32 v41, v46, v47, s48
	v_cvt_scalef32_pk_fp8_f32 v34, v52, v53, s48 op_sel:[0,0,0,1]
	v_cvt_scalef32_pk_fp8_f32 v38, v126, v127, s48 op_sel:[0,0,0,1]
	v_cvt_scalef32_pk_fp8_f32 v35, v56, v57, s48 op_sel:[0,0,0,1]
	v_cvt_scalef32_pk_fp8_f32 v39, v148, v149, s48 op_sel:[0,0,0,1]
	v_cvt_scalef32_pk_fp8_f32 v36, v60, v61, s48 op_sel:[0,0,0,1]
	v_cvt_scalef32_pk_fp8_f32 v40, v44, v45, s48 op_sel:[0,0,0,1]
	v_cvt_scalef32_pk_fp8_f32 v37, v64, v65, s48 op_sel:[0,0,0,1]
	s_waitcnt lgkmcnt(4)
	v_mfma_f32_32x32x64_f8f6f4 v[82:97], v[82:89], v[98:105], 0
	v_cvt_scalef32_pk_fp8_f32 v41, v48, v49, s48 op_sel:[0,0,0,1]
	v_add_f32_e64 v110, v110, v52
	v_add_f32_e64 v111, v111, v53
	v_add_f32_e64 v50, v108, v50
	v_add_f32_e64 v51, v109, v51
	s_addk_i32 s6, 0x4680
	v_add_f32_e64 v52, v56, v110
	v_add_f32_e64 v53, v57, v111
	v_add_f32_e64 v50, v54, v50
	v_add_f32_e64 v51, v55, v51
	s_cmp_lg_u32 s8, 2
	v_add_f32_e64 v50, v58, v50
	v_add_f32_e64 v51, v59, v51
	v_pk_add_f32 v[52:53], v[60:61], v[52:53]
	s_cselect_b32 s4, s6, 0
	v_pk_add_f32 v[52:53], v[64:65], v[52:53]
	v_pk_add_f32 v[50:51], v[62:63], v[50:51]
	s_add_i32 s4, s4, 0
	v_pk_add_f32 v[50:51], v[124:125], v[50:51]
	v_pk_add_f32 v[52:53], v[126:127], v[52:53]
	s_waitcnt lgkmcnt(2)
	v_mfma_f32_32x32x64_f8f6f4 v[18:33], v[116:123], v[34:41], v[18:33]
	v_add_f32_e64 v52, v148, v52
	v_add_f32_e64 v53, v149, v53
	v_add_f32_e64 v50, v146, v50
	v_add_f32_e64 v51, v147, v51
	v_add_f32_e64 v44, v44, v52
	v_add_f32_e64 v45, v45, v53
	v_add_f32_e64 v42, v42, v50
	v_add_f32_e64 v43, v43, v51
	v_add_f32_e64 v110, v48, v44
	v_add_f32_e64 v111, v49, v45
	v_add_f32_e64 v108, v46, v42
	v_add_f32_e64 v109, v47, v43
	s_nop 0
	s_nop 0
	s_nop 0
	s_nop 0
	s_nop 0
	s_nop 0
	s_nop 0
	s_nop 0
	s_waitcnt lgkmcnt(0)
	v_mfma_f32_32x32x64_f8f6f4 v[2:17], v[138:145], v[34:41], v[2:17]
	v_add_u32_e32 v34, s4, v155
	s_waitcnt vmcnt(3)
	ds_write_b64 v34, v[112:113]
	v_add_u32_e32 v34, s4, v156
	v_add_u32_e32 v34, 0x1400, v34
	s_waitcnt vmcnt(2)
	ds_write2_b32 v34, v114, v115 offset1:8
	s_nop 0
	s_nop 0
	s_nop 0
	s_nop 0
	s_nop 0
	s_nop 0
	s_nop 0
	s_nop 0
	s_waitcnt lgkmcnt(0)
	s_barrier

; DI f32x16 mfma8(v8i a, v8i b, f32x16 c) { return __builtin_amdgcn_mfma_scale_f32_32x32x64_f8f6f4(a, b, c, 0, 0, 0, 0, 0, 0); }
; DI void attn_unit_a8(unsigned char* lds, const AttnArgs& a) {
;     ...
;     auto step = [&](int t, u32x2& kl, u32x2& vl, const u32x2& ks, const u32x2& vs, f32x16& c0, f32x16& c1, f32x16& n0, f32x16& n1, const int hk, const int wj) __attribute__((always_inline)) {
;         const int slot1 = slot == 2 ? 0 : slot + 1, slot2 = slot1 == 2 ? 0 : slot1 + 1;
;         if (hk == 1) { w_cvt(); w_issue(wj + 1 < AT_NWT ? wj + 1 : AT_NWT - 1); }
;         if (hk == 2) w_store(wj);
;         { const int tn = t + 3; gload(tn < a.t1 ? tn : a.t1 - 1, kl, vl); }
;         const unsigned char* Kb = lds + slot * AT_BUFB; const unsigned char* Kn = lds + slot1 * AT_BUFB;
;         const v8i k0 = kread(Kn, 0), k1 = kread(Kn, 1), v0 = vread(Kb, 0), v1 = vread(Kb, 1);
;         n0 = mfma8(k0, qf8, cinit); n1 = mfma8(k1, qf8, cinit);
;         expsum(c0); expsum(c1);
;         const v8i P = pack8(c0, c1);
;         o0[0] = mfma8(v0, P, o0[0]); o0[1] = mfma8(v1, P, o0[1]);
;         lstore(slot2, ks, vs);
;         __syncthreads();
;         slot = slot1;
;     };
.LBB0_1933:
	s_lshl_b32 s10, s75, 8
	s_ashr_i32 s11, s10, 31
	s_lshl_b64 s[10:11], s[10:11], 7
	s_add_u32 s8, s54, s10
	s_addc_u32 s10, s55, s11
	s_add_u32 s8, s8, s77
	s_addc_u32 s10, s10, 0
	s_add_u32 s12, s8, 0x400000
	s_addc_u32 s13, s10, 0
	s_mov_b32 s14, 0
	v_mov_b64_e32 v[80:81], v[64:65]
	v_mov_b64_e32 v[78:79], v[62:63]
	v_mov_b64_e32 v[76:77], v[60:61]
	v_mov_b64_e32 v[74:75], v[58:59]
	v_mov_b64_e32 v[72:73], v[56:57]
	v_mov_b64_e32 v[70:71], v[54:55]
	v_mov_b64_e32 v[68:69], v[52:53]
	v_mov_b64_e32 v[66:67], v[50:51]
	v_mov_b64_e32 v[96:97], v[48:49]
	v_mov_b64_e32 v[94:95], v[46:47]
	v_mov_b64_e32 v[92:93], v[44:45]
	v_mov_b64_e32 v[90:91], v[42:43]
	v_mov_b64_e32 v[88:89], v[40:41]
	v_mov_b64_e32 v[86:87], v[38:39]
	v_mov_b64_e32 v[84:85], v[36:37]
	v_mov_b64_e32 v[82:83], v[34:35]
.LBB0_1934:
	s_min_u32 s8, s50, 64
	s_cmp_lt_u32 s50, 61
	s_cselect_b64 s[10:11], -1, 0
	s_lshl_b32 s8, s8, 6
	s_add_i32 s15, s8, 0xc0
	s_add_i32 s18, s8, 0xfffff0c0
	s_and_b64 s[16:17], s[10:11], exec
	s_cselect_b32 s15, s15, s18
	s_mov_b32 s18, s14
	s_add_i32 s14, s14, 1
	s_cmp_lg_u32 s18, 2
	s_cselect_b32 s14, s14, 0
	s_mul_i32 s19, s14, 0x4680
	s_nop 0
	v_add_u32_e32 v106, s19, v169
	s_nop 0
	s_nop 0
	s_nop 0
	s_nop 0
	s_nop 0
	s_nop 0
	s_nop 0
	ds_read_b128 v[50:53], v106
	ds_read_b128 v[54:57], v106 offset:16
	v_add_u32_e32 v58, s15, v130
	s_nop 0
	s_and_b64 s[10:11], s[10:11], exec
	v_ashrrev_i32_e32 v59, 31, v58
	s_nop 0
	s_nop 0
	s_nop 0
	s_nop 0
	s_nop 0
	s_nop 0
	s_nop 0
	s_cselect_b32 s16, s42, s12
	s_cselect_b32 s17, s43, s13
	s_waitcnt lgkmcnt(0)
	v_mfma_f32_32x32x64_f8f6f4 v[34:49], v[50:57], v[98:105], 0
	v_lshlrev_b64 v[50:51], 7, v[58:59]
	v_lshl_add_u64 v[50:51], s[16:17], 0, v[50:51]
	v_lshl_add_u64 v[50:51], v[50:51], 0, v[132:133]
	v_lshl_add_u64 v[58:59], v[134:135], 0, s[8:9]
	global_load_dwordx2 v[112:113], v[50:51], off
	ds_read_b128 v[50:53], v106 offset:2560
	ds_read_b128 v[54:57], v106 offset:2576
	global_load_dwordx2 v[114:115], v[58:59], off offset:192
	s_mulk_i32 s18, 0x4680
	v_add_u32_e32 v58, s18, v169
	v_exp_f32_e32 v82, v82
	v_exp_f32_e32 v83, v83
	v_exp_f32_e32 v86, v86
	v_exp_f32_e32 v87, v87
	v_exp_f32_e32 v90, v90
	v_exp_f32_e32 v91, v91
	v_exp_f32_e32 v94, v94
	v_exp_f32_e32 v95, v95
	v_exp_f32_e32 v124, v66
	v_exp_f32_e32 v125, v67
	v_exp_f32_e32 v148, v70
	v_exp_f32_e32 v149, v71
	v_exp_f32_e32 v74, v74
	v_exp_f32_e32 v75, v75
	v_exp_f32_e32 v78, v78
	v_exp_f32_e32 v79, v79
	ds_read_b128 v[116:119], v58 offset:5120
	ds_read_b128 v[120:123], v58 offset:5136
	ds_read_b128 v[140:143], v58 offset:7680
	ds_read_b128 v[144:147], v58 offset:7696
	v_exp_f32_e32 v84, v84
	v_exp_f32_e32 v85, v85
	v_exp_f32_e32 v88, v88
	v_exp_f32_e32 v89, v89
	v_exp_f32_e32 v92, v92
	v_exp_f32_e32 v93, v93
	v_exp_f32_e32 v96, v96
	v_exp_f32_e32 v97, v97
	v_exp_f32_e32 v126, v68
	v_exp_f32_e32 v127, v69
	v_exp_f32_e32 v150, v72
	v_exp_f32_e32 v151, v73
	v_exp_f32_e32 v76, v76
	v_exp_f32_e32 v77, v77
	v_exp_f32_e32 v80, v80
	v_exp_f32_e32 v81, v81
	s_nop 0
	s_nop 0
	s_nop 0
	s_nop 0
	s_nop 0
	s_nop 0
	s_nop 0
	s_nop 0
	v_cvt_scalef32_pk_fp8_f32 v66, v82, v83, s69
	v_cvt_scalef32_pk_fp8_f32 v70, v124, v125, s69
	v_cvt_scalef32_pk_fp8_f32 v67, v86, v87, s69
	v_cvt_scalef32_pk_fp8_f32 v71, v148, v149, s69
	v_cvt_scalef32_pk_fp8_f32 v68, v90, v91, s69
	v_cvt_scalef32_pk_fp8_f32 v72, v74, v75, s69
	v_cvt_scalef32_pk_fp8_f32 v69, v94, v95, s69
	v_cvt_scalef32_pk_fp8_f32 v73, v78, v79, s69
	v_cvt_scalef32_pk_fp8_f32 v66, v84, v85, s69 op_sel:[0,0,0,1]
	v_cvt_scalef32_pk_fp8_f32 v70, v126, v127, s69 op_sel:[0,0,0,1]
	v_cvt_scalef32_pk_fp8_f32 v67, v88, v89, s69 op_sel:[0,0,0,1]
	v_cvt_scalef32_pk_fp8_f32 v71, v150, v151, s69 op_sel:[0,0,0,1]
	v_cvt_scalef32_pk_fp8_f32 v68, v92, v93, s69 op_sel:[0,0,0,1]
	v_cvt_scalef32_pk_fp8_f32 v72, v76, v77, s69 op_sel:[0,0,0,1]
	v_cvt_scalef32_pk_fp8_f32 v69, v96, v97, s69 op_sel:[0,0,0,1]
	v_cvt_scalef32_pk_fp8_f32 v73, v80, v81, s69 op_sel:[0,0,0,1]
	s_waitcnt lgkmcnt(4)
	v_mfma_f32_32x32x64_f8f6f4 v[50:65], v[50:57], v[98:105], 0
	s_add_i32 s15, s19, 0x4680
	s_cmp_eq_u32 s14, 2
	v_add_f32_e64 v110, v110, v84
	v_add_f32_e64 v111, v111, v85
	v_add_f32_e64 v82, v108, v82
	v_add_f32_e64 v83, v109, v83
	s_cselect_b64 s[10:11], -1, 0
	v_add_f32_e64 v84, v88, v110
	v_add_f32_e64 v85, v89, v111
	v_add_f32_e64 v82, v86, v82
	v_add_f32_e64 v83, v87, v83
	v_add_f32_e64 v84, v92, v84
	v_add_f32_e64 v85, v93, v85
	v_pk_add_f32 v[82:83], v[90:91], v[82:83]
	s_and_b64 s[16:17], s[10:11], exec
	v_pk_add_f32 v[84:85], v[96:97], v[84:85]
	v_pk_add_f32 v[82:83], v[94:95], v[82:83]
	s_cselect_b32 s8, 0, s15
	v_pk_add_f32 v[82:83], v[124:125], v[82:83]
	v_pk_add_f32 v[84:85], v[126:127], v[84:85]
	s_waitcnt lgkmcnt(2)
	v_mfma_f32_32x32x64_f8f6f4 v[18:33], v[116:123], v[66:73], v[18:33]
	s_add_i32 s8, s8, 0
	v_add_f32_e64 v84, v150, v84
	v_add_f32_e64 v85, v151, v85
	v_add_f32_e64 v82, v148, v82
	v_add_f32_e64 v83, v149, v83
	v_add_f32_e64 v76, v76, v84
	v_add_f32_e64 v77, v77, v85
	v_add_f32_e64 v74, v74, v82
	v_add_f32_e64 v75, v75, v83
	v_add_f32_e64 v110, v80, v76
	v_add_f32_e64 v111, v81, v77
	v_add_f32_e64 v108, v78, v74
	v_add_f32_e64 v109, v79, v75
	s_cmpk_gt_u32 s50, 0x42
	s_waitcnt lgkmcnt(0)
	v_mfma_f32_32x32x64_f8f6f4 v[2:17], v[140:147], v[66:73], v[2:17]
	v_add_u32_e32 v66, s8, v131
	s_waitcnt vmcnt(3)
	ds_write_b64 v66, v[136:137]
	v_add_u32_e32 v66, s8, v168
	v_add_u32_e32 v66, 0x1400, v66
	s_waitcnt vmcnt(2)
	ds_write2_b32 v66, v138, v139 offset1:8
	s_waitcnt lgkmcnt(0)
	s_barrier
; DI f32x16 mfma8(v8i a, v8i b, f32x16 c) { return __builtin_amdgcn_mfma_scale_f32_32x32x64_f8f6f4(a, b, c, 0, 0, 0, 0, 0, 0); }
; DI void attn_unit_a8(unsigned char* lds, const AttnArgs& a) {
;     ...
;     auto step = [&](int t, u32x2& kl, u32x2& vl, const u32x2& ks, const u32x2& vs, f32x16& c0, f32x16& c1, f32x16& n0, f32x16& n1, const int hk, const int wj) __attribute__((always_inline)) {
;         const int slot1 = slot == 2 ? 0 : slot + 1, slot2 = slot1 == 2 ? 0 : slot1 + 1;
;         if (hk == 1) { w_cvt(); w_issue(wj + 1 < AT_NWT ? wj + 1 : AT_NWT - 1); }
;         if (hk == 2) w_store(wj);
;         { const int tn = t + 3; gload(tn < a.t1 ? tn : a.t1 - 1, kl, vl); }
;         const unsigned char* Kb = lds + slot * AT_BUFB; const unsigned char* Kn = lds + slot1 * AT_BUFB;
;         const v8i k0 = kread(Kn, 0), k1 = kread(Kn, 1), v0 = vread(Kb, 0), v1 = vread(Kb, 1);
;         n0 = mfma8(k0, qf8, cinit); n1 = mfma8(k1, qf8, cinit);
;         expsum(c0); expsum(c1);
;         const v8i P = pack8(c0, c1);
;         o0[0] = mfma8(v0, P, o0[0]); o0[1] = mfma8(v1, P, o0[1]);
;         lstore(slot2, ks, vs);
;         __syncthreads();
;         slot = slot1;
;     };
	s_cbranch_scc1 .LBB0_1936
	s_min_u32 s8, s50, 63
	s_cmp_lt_u32 s50, 60
	s_cselect_b64 s[16:17], -1, 0
	s_lshl_b32 s8, s8, 6
	s_add_i32 s15, s8, 0x100
	s_add_i32 s20, s8, 0xfffff100
	s_and_b64 s[18:19], s[16:17], exec
	s_cselect_b32 s15, s15, s20
	s_add_i32 s14, s14, 1
	s_and_b64 s[10:11], s[10:11], exec
	v_add_u32_e32 v82, s15, v130
	s_cselect_b32 s14, 0, s14
	s_and_b64 s[16:17], s[16:17], exec
	v_ashrrev_i32_e32 v83, 31, v82
	s_cselect_b32 s17, s43, s13
	s_cselect_b32 s16, s42, s12
	v_lshlrev_b64 v[82:83], 7, v[82:83]
	s_mul_i32 s10, s14, 0x4680
	v_lshl_add_u64 v[90:91], s[16:17], 0, v[82:83]
	v_add_u32_e32 v86, s10, v169
	v_lshl_add_u64 v[90:91], v[90:91], 0, v[132:133]
	ds_read_b128 v[66:69], v86 offset:2560
	ds_read_b128 v[70:73], v86 offset:2576
	ds_read_b128 v[82:85], v86
	ds_read_b128 v[86:89], v86 offset:16
	global_load_dwordx2 v[136:137], v[90:91], off
	v_lshl_add_u64 v[90:91], v[134:135], 0, s[8:9]
	global_load_dwordx2 v[138:139], v[90:91], off offset:256
	v_exp_f32_e32 v124, v34
	v_exp_f32_e32 v125, v35
	v_exp_f32_e32 v36, v36
	v_exp_f32_e32 v37, v37
	v_exp_f32_e32 v126, v38
	v_exp_f32_e32 v127, v39
	v_exp_f32_e32 v42, v42
	v_exp_f32_e32 v43, v43
	v_exp_f32_e32 v46, v46
	v_exp_f32_e32 v47, v47
	v_exp_f32_e32 v50, v50
	v_exp_f32_e32 v51, v51
	v_exp_f32_e32 v54, v54
	v_exp_f32_e32 v55, v55
	v_exp_f32_e32 v58, v58
	v_exp_f32_e32 v59, v59
	v_exp_f32_e32 v62, v62
	v_exp_f32_e32 v63, v63
	ds_read_b128 v[116:119], v106 offset:5120
	ds_read_b128 v[120:123], v106 offset:5136
	ds_read_b128 v[140:143], v106 offset:7680
	ds_read_b128 v[144:147], v106 offset:7696
	v_exp_f32_e32 v148, v40
	v_exp_f32_e32 v149, v41
	v_exp_f32_e32 v44, v44
	v_exp_f32_e32 v45, v45
	v_exp_f32_e32 v48, v48
	v_exp_f32_e32 v49, v49
	v_exp_f32_e32 v52, v52
	v_exp_f32_e32 v53, v53
	v_exp_f32_e32 v56, v56
	v_exp_f32_e32 v57, v57
	v_exp_f32_e32 v60, v60
	v_exp_f32_e32 v61, v61
	v_exp_f32_e32 v64, v64
	v_exp_f32_e32 v65, v65
	s_nop 0
	v_cvt_scalef32_pk_fp8_f32 v34, v124, v125, s69
	v_pk_add_f32 v[110:111], v[110:111], v[36:37]
	v_cvt_scalef32_pk_fp8_f32 v34, v36, v37, s69 op_sel:[0,0,0,1]
	s_nop 0
	s_nop 0
	s_nop 0
	s_nop 0
	s_nop 0
	s_nop 0
	s_nop 0
	s_waitcnt lgkmcnt(6)
	v_mfma_f32_32x32x64_f8f6f4 v[66:81], v[66:73], v[98:105], 0
	v_cvt_scalef32_pk_fp8_f32 v38, v50, v51, s69
	v_cvt_scalef32_pk_fp8_f32 v35, v126, v127, s69
	v_cvt_scalef32_pk_fp8_f32 v39, v54, v55, s69
	v_cvt_scalef32_pk_fp8_f32 v36, v42, v43, s69
	v_cvt_scalef32_pk_fp8_f32 v40, v58, v59, s69
	v_cvt_scalef32_pk_fp8_f32 v37, v46, v47, s69
	v_cvt_scalef32_pk_fp8_f32 v41, v62, v63, s69
	v_cvt_scalef32_pk_fp8_f32 v38, v52, v53, s69 op_sel:[0,0,0,1]
	v_cvt_scalef32_pk_fp8_f32 v35, v148, v149, s69 op_sel:[0,0,0,1]
	v_cvt_scalef32_pk_fp8_f32 v39, v56, v57, s69 op_sel:[0,0,0,1]
	v_cvt_scalef32_pk_fp8_f32 v36, v44, v45, s69 op_sel:[0,0,0,1]
	v_cvt_scalef32_pk_fp8_f32 v40, v60, v61, s69 op_sel:[0,0,0,1]
	v_cvt_scalef32_pk_fp8_f32 v37, v48, v49, s69 op_sel:[0,0,0,1]
	v_cvt_scalef32_pk_fp8_f32 v41, v64, v65, s69 op_sel:[0,0,0,1]
	v_pk_add_f32 v[108:109], v[108:109], v[124:125]
	s_waitcnt lgkmcnt(4)
	v_mfma_f32_32x32x64_f8f6f4 v[82:97], v[82:89], v[98:105], 0
	s_addk_i32 s10, 0x4680
	v_add_f32_e64 v110, v148, v110
	v_add_f32_e64 v111, v149, v111
	v_add_f32_e64 v108, v126, v108
	v_add_f32_e64 v109, v127, v109
	s_cmp_lg_u32 s14, 2
	v_add_f32_e64 v42, v42, v108
	v_add_f32_e64 v43, v43, v109
	v_add_f32_e64 v44, v44, v110
	v_add_f32_e64 v45, v45, v111
	s_cselect_b32 s8, s10, 0
	v_add_f32_e64 v44, v48, v44
	v_add_f32_e64 v45, v49, v45
	v_pk_add_f32 v[42:43], v[46:47], v[42:43]
	s_add_i32 s8, s8, 0
	v_pk_add_f32 v[42:43], v[50:51], v[42:43]
	v_pk_add_f32 v[44:45], v[52:53], v[44:45]
	v_pk_add_f32 v[42:43], v[54:55], v[42:43]
	v_pk_add_f32 v[44:45], v[56:57], v[44:45]
	v_pk_add_f32 v[42:43], v[58:59], v[42:43]
	s_waitcnt lgkmcnt(2)
	v_mfma_f32_32x32x64_f8f6f4 v[18:33], v[116:123], v[34:41], v[18:33]
	v_add_f32_e64 v44, v60, v44
	v_add_f32_e64 v45, v61, v45
	v_add_f32_e64 v108, v62, v42
	v_add_f32_e64 v109, v63, v43
	v_add_f32_e64 v110, v64, v44
	v_add_f32_e64 v111, v65, v45
	s_nop 0
	s_nop 0
	s_nop 0
	s_nop 0
	s_nop 0
	s_nop 0
	s_nop 0
	s_nop 0
	s_waitcnt lgkmcnt(0)
	v_mfma_f32_32x32x64_f8f6f4 v[2:17], v[140:147], v[34:41], v[2:17]
	v_add_u32_e32 v34, s8, v131
	s_waitcnt vmcnt(3)
	ds_write_b64 v34, v[112:113]
	v_add_u32_e32 v34, s8, v168
	v_add_u32_e32 v34, 0x1400, v34
	s_waitcnt vmcnt(2)
	ds_write2_b32 v34, v114, v115 offset1:8
	s_nop 0
	s_nop 0
	s_nop 0
	s_nop 0
	s_nop 0
	s_nop 0
	s_nop 0
	s_nop 0
	s_waitcnt lgkmcnt(0)
	s_barrier
